# MoBA gate phase: the 12 block-mean/q loads of an item requested together (was three serial load+vmcnt(0) waves); on top of MoBA prologue and Wo epilogue de-serialisation
# speedup vs baseline: 1.0263x; 1.0035x over previous
.LBB0_341:
	s_and_b32 s26, s11, 31
	s_cmp_eq_u32 s26, 0
	v_lshl_add_u32 v24, s26, 8, v26
	s_cbranch_scc1 .LBB0_571
	s_ashr_i32 s12, s11, 9
	v_lshl_add_u32 v4, s12, 13, v24
	v_mov_b64_e32 v[2:3], s[8:9]
	s_movk_i32 s0, 0x1800
	v_mad_i64_i32 v[2:3], s[0:1], v4, s0, v[2:3]
	s_bfe_u32 s0, s11, 0x40005
	s_lshl_b32 s1, s12, 4
	s_lshl_b32 s56, s0, 7
	s_or_b32 s0, s1, s0
	s_ashr_i32 s1, s0, 31
	v_lshl_add_u64 v[2:3], v[2:3], 0, s[56:57]
	s_lshl_b64 s[0:1], s[0:1], 13
	v_lshl_add_u64 v[2:3], v[2:3], 0, v[0:1]
	v_lshl_add_u64 v[60:61], v[22:23], 0, s[0:1]
	global_load_dwordx4 v[18:21], v[2:3], off offset:96
	global_load_dwordx4 v[44:47], v[2:3], off offset:64
	global_load_dwordx4 v[48:51], v[2:3], off offset:32
	s_nop 0
	global_load_dwordx4 v[2:5], v[2:3], off
	s_nop 0
	global_load_dwordx4 v[6:9], v[60:61], off offset:16
	global_load_dwordx4 v[10:13], v[60:61], off
	global_load_dwordx4 v[52:55], v[60:61], off offset:80
	global_load_dwordx4 v[56:59], v[60:61], off offset:64
	global_load_dwordx4 v[190:193], v[60:61], off offset:144
	global_load_dwordx4 v[194:197], v[60:61], off offset:128
	global_load_dwordx4 v[198:201], v[60:61], off offset:208
	global_load_dwordx4 v[202:205], v[60:61], off offset:192
	v_cmp_gt_u32_e64 s[0:1], s26, v27
	s_mov_b32 s12, 0xff800000
	s_mov_b64 s[16:17], -1
	s_waitcnt vmcnt(4)
	v_cvt_pk_bf16_f32 v10, v10, v11
	v_cvt_pk_bf16_f32 v11, v12, v13
	v_cvt_pk_bf16_f32 v12, v6, v7
	v_cvt_pk_bf16_f32 v13, v8, v9
	v_cvt_pk_bf16_f32 v56, v56, v57
	v_cvt_pk_bf16_f32 v57, v58, v59
	v_mfma_f32_32x32x16_bf16 v[2:17], v[10:13], v[2:5], 0
	v_cvt_pk_bf16_f32 v58, v52, v53
	v_cvt_pk_bf16_f32 v59, v54, v55
	s_nop 1
	v_mfma_f32_32x32x16_bf16 v[2:17], v[56:59], v[48:51], v[2:17]
	s_waitcnt vmcnt(2)
	v_cvt_pk_bf16_f32 v52, v194, v195
	v_cvt_pk_bf16_f32 v53, v196, v197
	v_cvt_pk_bf16_f32 v54, v190, v191
	v_cvt_pk_bf16_f32 v55, v192, v193
	s_nop 1
	v_mfma_f32_32x32x16_bf16 v[2:17], v[52:55], v[44:47], v[2:17]
	s_waitcnt vmcnt(0)
	v_cvt_pk_bf16_f32 v48, v202, v203
	v_cvt_pk_bf16_f32 v49, v204, v205
	v_cvt_pk_bf16_f32 v50, v198, v199
	v_cvt_pk_bf16_f32 v51, v200, v201
	s_nop 1
	v_mfma_f32_32x32x16_bf16 v[2:17], v[48:51], v[18:21], v[2:17]
	s_nop 11
	v_cndmask_b32_e64 v2, v228, v2, s[0:1]
	v_cmp_nlg_f32_e64 s[40:41], s12, v2
	s_mov_b64 s[12:13], -1
	s_and_saveexec_b64 s[14:15], s[40:41]
	s_cbranch_execz .LBB0_346
	s_mov_b32 s16, 0xff800000
	v_cmp_eq_f32_e64 s[42:43], s16, v2
	s_mov_b64 s[16:17], 0
	s_and_saveexec_b64 s[18:19], s[42:43]
	s_and_b64 s[16:17], s[0:1], exec
	s_or_b64 exec, exec, s[18:19]
	s_orn2_b64 s[16:17], s[16:17], exec
